# also: P8 epilogue requests all 16 slot words before its first wait
# speedup vs baseline: 1.0108x; 1.0006x over previous
.LBB0_943:
	s_lshl_b32 s25, s34, 6
	s_add_i32 s36, s25, s36
	s_ashr_i32 s37, s36, 31
	s_lshl_b64 s[36:37], s[36:37], 16
	v_lshl_add_u64 v[0:1], v[170:171], 0, s[36:37]
	v_add_co_u32_e32 v2, vcc, 0x1000, v0
	s_nop 1
	v_addc_co_u32_e32 v3, vcc, 0, v1, vcc
	v_add_co_u32_e32 v4, vcc, 0x2000, v0
	s_nop 1
	v_addc_co_u32_e32 v5, vcc, 0, v1, vcc
	v_add_co_u32_e32 v6, vcc, 0x3000, v0
	s_nop 1
	v_addc_co_u32_e32 v7, vcc, 0, v1, vcc
	global_load_dwordx2 v[182:183], v[0:1], off
	global_load_dwordx2 v[30:31], v[2:3], off
	global_load_dwordx2 v[28:29], v[4:5], off
	global_load_dwordx2 v[26:27], v[6:7], off
	v_add_co_u32_e32 v2, vcc, 0x4000, v0
	s_nop 1
	v_addc_co_u32_e32 v3, vcc, 0, v1, vcc
	v_add_co_u32_e32 v4, vcc, 0x5000, v0
	s_nop 1
	v_addc_co_u32_e32 v5, vcc, 0, v1, vcc
	v_add_co_u32_e32 v6, vcc, 0x6000, v0
	s_nop 1
	v_addc_co_u32_e32 v7, vcc, 0, v1, vcc
	v_add_co_u32_e32 v8, vcc, 0x7000, v0
	s_nop 1
	v_addc_co_u32_e32 v9, vcc, 0, v1, vcc
	global_load_dwordx2 v[24:25], v[2:3], off
	global_load_dwordx2 v[22:23], v[4:5], off
	global_load_dwordx2 v[20:21], v[6:7], off
	global_load_dwordx2 v[18:19], v[8:9], off
	v_add_co_u32_e32 v2, vcc, 0x8000, v0
	s_nop 1
	v_addc_co_u32_e32 v3, vcc, 0, v1, vcc
	v_add_co_u32_e32 v4, vcc, 0x9000, v0
	s_nop 1
	v_addc_co_u32_e32 v5, vcc, 0, v1, vcc
	v_add_co_u32_e32 v6, vcc, 0xa000, v0
	s_nop 1
	v_addc_co_u32_e32 v7, vcc, 0, v1, vcc
	v_add_co_u32_e32 v8, vcc, 0xb000, v0
	s_nop 1
	v_addc_co_u32_e32 v9, vcc, 0, v1, vcc
	global_load_dwordx2 v[16:17], v[2:3], off
	global_load_dwordx2 v[14:15], v[4:5], off
	global_load_dwordx2 v[12:13], v[6:7], off
	global_load_dwordx2 v[10:11], v[8:9], off
	v_add_co_u32_e32 v2, vcc, 0xc000, v0
	s_nop 1
	v_addc_co_u32_e32 v3, vcc, 0, v1, vcc
	v_add_co_u32_e32 v4, vcc, 0xd000, v0
	s_nop 1
	v_addc_co_u32_e32 v5, vcc, 0, v1, vcc
	v_add_co_u32_e32 v180, vcc, 0xe000, v0
	s_nop 1
	v_addc_co_u32_e32 v181, vcc, 0, v1, vcc
	v_add_co_u32_e32 v0, vcc, 0xf000, v0
	s_nop 1
	v_addc_co_u32_e32 v1, vcc, 0, v1, vcc
	global_load_dwordx2 v[8:9], v[2:3], off
	global_load_dwordx2 v[6:7], v[4:5], off
	s_nop 0
	global_load_dwordx2 v[2:3], v[180:181], off
	s_nop 0
	global_load_dwordx2 v[0:1], v[0:1], off
	v_lshl_add_u32 v4, s34, 8, v188
	v_ashrrev_i32_e32 v5, 31, v4
	v_lshlrev_b64 v[180:181], 9, v[4:5]
	v_lshl_add_u64 v[180:181], s[10:11], 0, v[180:181]
	s_waitcnt vmcnt(0)
	v_or_b32_e32 v168, v182, v183
	v_cmp_ne_u32_e32 vcc, 0, v168
	s_and_saveexec_b64 s[34:35], vcc
	s_mov_b32 s64, s66
	s_cbranch_execz .LBB0_953
	v_cmp_ne_u32_sdwa s[38:39], v182, v169 src0_sel:BYTE_0 src1_sel:DWORD
	s_and_saveexec_b64 s[36:37], s[38:39]
	s_cbranch_execnz .LBB0_1106
	s_or_b64 exec, exec, s[36:37]
	v_cmp_ne_u32_sdwa s[38:39], v182, v169 src0_sel:BYTE_1 src1_sel:DWORD
	s_and_saveexec_b64 s[36:37], s[38:39]
	s_cbranch_execnz .LBB0_1107
